# agg2 tail split: third-round nodes go one per wave, edge list cut over the 4 groups, online-softmax partials merged with ds_bpermute
# baseline (speedup 1.0000x reference)
_Z5k_aggILi1ELi40ELi5ELi5ELb1EEvPKiPKtPKDF16_PKfS7_S7_PvS5_S7_S7_PDF16_PfSA_:
	v_lshrrev_b32_e32 v46, 6, v0
	s_lshl_b32 s3, s2, 2
	v_readfirstlane_b32 s25, v46
	s_load_dwordx4 s[4:7], s[0:1], 0x0
	s_load_dwordx2 s[8:9], s[0:1], 0x10
	s_load_dwordx2 s[12:13], s[0:1], 0x20
	s_load_dwordx4 s[16:19], s[0:1], 0x28
	s_load_dword s20, s[0:1], 0x68
	s_add_i32 s25, s25, s3
	s_cmpk_ge_i32 s25, 0x30d4
	s_cbranch_scc1 .Lagg2n_end
	v_and_b32_e32 v52, 15, v0
	v_bfe_u32 v53, v0, 4, 2
	v_lshrrev_b32_e32 v54, 3, v52
	v_and_b32_e32 v55, 7, v52
	v_min_u32_e32 v47, 5, v55
	v_lshlrev_b32_e32 v56, 4, v47
	v_lshl_or_b32 v47, v46, 2, v53
	v_mul_u32_u24_e32 v47, 0x110, v47
	v_lshl_add_u32 v57, v52, 2, v47
	v_lshl_add_u32 v58, v54, 4, v47
	v_cmp_gt_u32_e32 vcc, 5, v52
	v_min_u32_e32 v47, 4, v55
	v_lshlrev_b32_e32 v47, 5, v47
	s_mov_b64 s[26:27], vcc
	v_mov_b32_e32 v51, 0xff800000
	v_mul_u32_u24_e32 v50, 0xa0, v46
	v_add_u32_e32 v50, v50, v47
	v_add_u32_e32 v50, 0x1100, v50
	v_and_b32_e32 v49, 63, v0
	v_cmp_gt_u32_e64 s[34:35], 5, v49
	s_waitcnt lgkmcnt(0)
	s_add_u32 s12, s12, 0x1da1c0
	s_addc_u32 s13, s13, 0
	s_lshl_b32 s11, s20, 2
	s_mov_b32 s36, 0
	s_mov_b32 s37, s25
	s_lshl_b32 s28, s11, 3
	s_sub_i32 s39, 0xc350, s28
	s_add_i32 s38, s28, s37
	s_min_i32 s38, s38, 0xc34f
	global_load_dwordx4 v[8:11], v47, s[16:17]
	global_load_dwordx4 v[12:15], v47, s[16:17] offset:16
	v_lshl_or_b32 v59, s25, 2, v53
	v_lshlrev_b32_e32 v47, 2, v59
	global_load_dwordx2 v[60:61], v47, s[4:5]
	s_add_i32 s28, s25, s11
	s_min_i32 s28, s28, 0x30d3
	v_lshl_or_b32 v48, s28, 2, v53
	v_lshlrev_b32_e32 v47, 2, v48
	global_load_dwordx2 v[62:63], v47, s[4:5]
	v_lshlrev_b32_e32 v47, 1, v59
	global_load_ushort v70, v47, s[12:13]
	s_waitcnt vmcnt(2)
	v_add_u32_e32 v46, -1, v61
	v_add_u32_e32 v47, v60, v52
	v_min_i32_e32 v48, v47, v46
	v_max_i32_e32 v48, 0, v48
	v_lshlrev_b32_e32 v48, 1, v48
	global_load_ushort v66, v48, s[6:7]
	v_add_u32_e32 v48, 16, v47
	v_min_i32_e32 v48, v48, v46
	v_max_i32_e32 v48, 0, v48
	v_lshlrev_b32_e32 v48, 1, v48
	global_load_ushort v67, v48, s[6:7]
	v_add_u32_e32 v48, 32, v47
	v_min_i32_e32 v48, v48, v46
	v_max_i32_e32 v48, 0, v48
	v_lshlrev_b32_e32 v48, 1, v48
	global_load_ushort v68, v48, s[6:7]
	v_add_u32_e32 v48, 48, v47
	v_min_i32_e32 v48, v48, v46
	v_max_i32_e32 v48, 0, v48
	v_lshlrev_b32_e32 v48, 1, v48
	global_load_ushort v69, v48, s[6:7]
	s_waitcnt vmcnt(0)
	s_and_saveexec_b64 s[28:29], s[34:35]
	ds_write_b128 v50, v[8:11]
	ds_write_b128 v50, v[12:15] offset:16
	s_mov_b64 exec, s[28:29]
.Lagg2n_quad:
	v_cvt_f32_f16_e32 v71, v70
	v_lshlrev_b32_e32 v46, 7, v66
	v_lshlrev_b32_e32 v47, 7, v67
	v_lshlrev_b32_e32 v48, 7, v68
	v_lshlrev_b32_e32 v49, 7, v69
	ds_write2_b32 v57, v46, v47 offset1:16
	ds_write2_b32 v57, v48, v49 offset0:32 offset1:48
	v_sub_u32_e32 v72, v61, v60
	v_mov_b32_e32 v46, s38
	v_lshlrev_b32_e32 v46, 2, v46
	global_load_dwordx2 v[64:65], v46, s[4:5]
	s_cmp_eq_u32 s36, 1
	s_cbranch_scc0 .Lagg2n_nosplit
	v_sub_u32_e32 v46, v63, v62
	v_add_u32_e32 v46, 3, v46
	v_lshrrev_b32_e32 v46, 2, v46
	v_mul_u32_u24_e32 v47, v53, v46
	v_add_u32_e32 v47, v62, v47
	v_min_i32_e32 v62, v47, v63
	v_add_u32_e32 v47, v62, v46
	v_min_i32_e32 v63, v47, v63
.Lagg2n_nosplit:
	v_add_u32_e32 v46, -1, v63
	v_add_u32_e32 v47, v62, v52
	v_min_i32_e32 v48, v47, v46
	v_max_i32_e32 v48, 0, v48
	v_lshlrev_b32_e32 v48, 1, v48
	global_load_ushort v66, v48, s[6:7]
	v_add_u32_e32 v48, 16, v47
	v_min_i32_e32 v48, v48, v46
	v_max_i32_e32 v48, 0, v48
	v_lshlrev_b32_e32 v48, 1, v48
	global_load_ushort v67, v48, s[6:7]
	v_add_u32_e32 v48, 32, v47
	v_min_i32_e32 v48, v48, v46
	v_max_i32_e32 v48, 0, v48
	v_lshlrev_b32_e32 v48, 1, v48
	global_load_ushort v68, v48, s[6:7]
	v_add_u32_e32 v48, 48, v47
	v_min_i32_e32 v48, v48, v46
	v_max_i32_e32 v48, 0, v48
	v_lshlrev_b32_e32 v48, 1, v48
	global_load_ushort v69, v48, s[6:7]
	s_add_i32 s28, s37, s11
	v_lshl_or_b32 v47, s28, 2, v53
	v_mov_b32_e32 v46, s38
	s_cmp_eq_u32 s36, 0
	s_cselect_b64 s[28:29], -1, 0
	v_cndmask_b32_e64 v46, v46, v47, s[28:29]
	v_lshlrev_b32_e32 v46, 1, v46
	global_load_ushort v70, v46, s[12:13]
	v_readlane_b32 s30, v72, 0
	v_readlane_b32 s31, v72, 16
	v_readlane_b32 s32, v72, 32
	v_readlane_b32 s33, v72, 48
	v_mov_b32_e32 v24, 0
	v_mov_b32_e32 v25, 0
	v_mov_b32_e32 v26, 0
	v_mov_b32_e32 v27, 0
	v_mov_b32_e32 v28, 0
	v_mov_b32_e32 v29, 0
	v_mov_b32_e32 v30, 0
	v_mov_b32_e32 v31, 0
	v_mov_b32_e32 v32, 0
	v_mov_b32_e32 v33, 0xff800000
	s_max_i32 s30, s30, s31
	s_max_i32 s32, s32, s33
	s_max_i32 s21, s30, s32
	s_mov_b32 s22, 0

.Lagg2n_epi:
	ds_read_b128 v[8:11], v50
	ds_read_b128 v[12:15], v50 offset:16
	v_add_f32_dpp v24, v24, v24 row_ror:8 row_mask:0xf bank_mask:0xf
	v_add_f32_dpp v25, v25, v25 row_ror:8 row_mask:0xf bank_mask:0xf
	v_add_f32_dpp v26, v26, v26 row_ror:8 row_mask:0xf bank_mask:0xf
	v_add_f32_dpp v27, v27, v27 row_ror:8 row_mask:0xf bank_mask:0xf
	v_add_f32_dpp v28, v28, v28 row_ror:8 row_mask:0xf bank_mask:0xf
	v_add_f32_dpp v29, v29, v29 row_ror:8 row_mask:0xf bank_mask:0xf
	v_add_f32_dpp v30, v30, v30 row_ror:8 row_mask:0xf bank_mask:0xf
	v_add_f32_dpp v31, v31, v31 row_ror:8 row_mask:0xf bank_mask:0xf
	v_add_f32_dpp v32, v32, v32 row_ror:8 row_mask:0xf bank_mask:0xf
	s_cmp_eq_u32 s36, 2
	s_cbranch_scc0 .Lagg2n_nomerge
	v_mbcnt_lo_u32_b32 v0, -1, 0
	v_mbcnt_hi_u32_b32 v0, -1, v0
	v_add_u32_e32 v1, 16, v0
	v_and_b32_e32 v1, 63, v1
	v_lshlrev_b32_e32 v1, 2, v1
	v_add_u32_e32 v2, 32, v0
	v_and_b32_e32 v2, 63, v2
	v_lshlrev_b32_e32 v2, 2, v2
	v_add_u32_e32 v3, 48, v0
	v_and_b32_e32 v3, 63, v3
	v_lshlrev_b32_e32 v3, 2, v3
	v_cmp_lt_f32_e32 vcc, 0, v32
	s_nop 1
	v_cndmask_b32_e32 v4, v51, v33, vcc
	s_nop 0
	ds_bpermute_b32 v5, v1, v4
	ds_bpermute_b32 v6, v2, v4
	ds_bpermute_b32 v7, v3, v4
	s_waitcnt lgkmcnt(0)
	v_max3_f32 v5, v5, v6, v7
	v_max_f32_e32 v5, v5, v4
	v_cmp_neq_f32_e32 vcc, 0xff800000, v5
	s_nop 1
	v_cndmask_b32_e32 v5, 0, v5, vcc
	v_sub_f32_e32 v4, v4, v5
	v_exp_f32_e32 v4, v4
	s_nop 0
	v_mul_f32_e32 v24, v24, v4
	v_mul_f32_e32 v25, v25, v4
	v_mul_f32_e32 v26, v26, v4
	v_mul_f32_e32 v27, v27, v4
	v_mul_f32_e32 v28, v28, v4
	v_mul_f32_e32 v29, v29, v4
	v_mul_f32_e32 v30, v30, v4
	v_mul_f32_e32 v31, v31, v4
	v_mul_f32_e32 v32, v32, v4
	s_nop 0
	ds_bpermute_b32 v5, v1, v24
	ds_bpermute_b32 v6, v2, v24
	ds_bpermute_b32 v7, v3, v24
	ds_bpermute_b32 v34, v1, v25
	ds_bpermute_b32 v35, v2, v25
	ds_bpermute_b32 v36, v3, v25
	ds_bpermute_b32 v37, v1, v26
	ds_bpermute_b32 v38, v2, v26
	ds_bpermute_b32 v39, v3, v26
	ds_bpermute_b32 v40, v1, v27
	ds_bpermute_b32 v41, v2, v27
	ds_bpermute_b32 v42, v3, v27
	ds_bpermute_b32 v43, v1, v28
	ds_bpermute_b32 v44, v2, v28
	ds_bpermute_b32 v45, v3, v28
	s_waitcnt lgkmcnt(0)
	v_add_f32_e32 v5, v5, v6
	v_add_f32_e32 v24, v24, v7
	v_add_f32_e32 v24, v24, v5
	v_add_f32_e32 v34, v34, v35
	v_add_f32_e32 v25, v25, v36
	v_add_f32_e32 v25, v25, v34
	v_add_f32_e32 v37, v37, v38
	v_add_f32_e32 v26, v26, v39
	v_add_f32_e32 v26, v26, v37
	v_add_f32_e32 v40, v40, v41
	v_add_f32_e32 v27, v27, v42
	v_add_f32_e32 v27, v27, v40
	v_add_f32_e32 v43, v43, v44
	v_add_f32_e32 v28, v28, v45
	v_add_f32_e32 v28, v28, v43
	s_nop 0
	ds_bpermute_b32 v5, v1, v29
	ds_bpermute_b32 v6, v2, v29
	ds_bpermute_b32 v7, v3, v29
	ds_bpermute_b32 v34, v1, v30
	ds_bpermute_b32 v35, v2, v30
	ds_bpermute_b32 v36, v3, v30
	ds_bpermute_b32 v37, v1, v31
	ds_bpermute_b32 v38, v2, v31
	ds_bpermute_b32 v39, v3, v31
	ds_bpermute_b32 v40, v1, v32
	ds_bpermute_b32 v41, v2, v32
	ds_bpermute_b32 v42, v3, v32
	s_waitcnt lgkmcnt(0)
	v_add_f32_e32 v5, v5, v6
	v_add_f32_e32 v29, v29, v7
	v_add_f32_e32 v29, v29, v5
	v_add_f32_e32 v34, v34, v35
	v_add_f32_e32 v30, v30, v36
	v_add_f32_e32 v30, v30, v34
	v_add_f32_e32 v37, v37, v38
	v_add_f32_e32 v31, v31, v39
	v_add_f32_e32 v31, v31, v37
	v_add_f32_e32 v40, v40, v41
	v_add_f32_e32 v32, v32, v42
	v_add_f32_e32 v32, v32, v40
.Lagg2n_nomerge:
	v_mov_b32_e32 v60, v62
	v_mov_b32_e32 v61, v63
	v_mov_b32_e32 v62, v64
	v_mov_b32_e32 v63, v65
	v_rcp_f32_e32 v46, v32
	v_cmp_lt_f32_e32 vcc, 0, v32
	v_mul_u32_u24_e32 v47, 0xa0, v59
	v_lshl_add_u32 v47, v55, 5, v47
	v_cndmask_b32_e32 v46, 0, v46, vcc
	s_waitcnt lgkmcnt(0)
	v_fma_f32 v0, v24, v46, v8
	v_fma_f32 v1, v25, v46, v9
	v_fma_f32 v2, v26, v46, v10
	v_fma_f32 v3, v27, v46, v11
	v_fma_f32 v4, v28, v46, v12
	v_fma_f32 v5, v29, v46, v13
	v_fma_f32 v6, v30, v46, v14
	v_fma_f32 v7, v31, v46, v15
	s_and_b64 s[30:31], s[26:27], 0xffff
	s_cmp_eq_u32 s36, 2
	s_cselect_b64 s[30:31], s[30:31], s[26:27]
	s_and_saveexec_b64 s[28:29], s[30:31]
	global_store_dwordx4 v47, v[0:3], s[18:19] nt
	global_store_dwordx4 v47, v[4:7], s[18:19] offset:16 nt
	s_mov_b64 exec, s[28:29]
	s_add_i32 s36, s36, 1
	s_cmp_eq_u32 s36, 1
	s_cbranch_scc0 .Lagg2n_r2
	s_add_i32 s25, s37, s11
	v_lshl_or_b32 v59, s25, 2, v53
	s_branch .Lagg2n_quad
.Lagg2n_r2:
	s_cmp_eq_u32 s36, 2
	s_cbranch_scc0 .Lagg2n_end
	s_cmp_lt_i32 s37, s39
	s_cbranch_scc0 .Lagg2n_end
	v_mov_b32_e32 v59, s38
	s_branch .Lagg2n_quad
